# v62 + P11 per-query instruction trims: lane constants hoisted out of the query loop (100 instr), direct fp8->bf16 q' conversion (31), dead zero-inits (13)
# speedup vs baseline: 1.0117x; 1.0025x over previous
.LBB0_1449:
	s_or_b64 exec, exec, s[16:17]
	v_ashrrev_i32_e32 v1, 31, v0
	v_lshl_add_u64 v[2:3], v[0:1], 2, s[14:15]
	global_load_dword v2, v[2:3], off
	v_lshl_add_u32 v1, v0, 2, 0
	v_add_u32_e32 v1, 0x24000, v1
	v_cmp_gt_i32_e32 vcc, 16, v0
	s_waitcnt vmcnt(0)
	v_mul_f32_e32 v2, 0x3fb8aa3b, v2
	ds_write_b32 v1, v2
	s_and_saveexec_b64 s[2:3], vcc
	v_mov_b32_e32 v0, 0xff800000
	ds_write_b32 v1, v0 offset:2048
	s_or_b64 exec, exec, s[2:3]
	s_lshl_b32 s2, s93, 14
	s_add_i32 s23, s2, 0
	s_lshl_b32 s2, s88, 3
	s_add_i32 s15, s2, s93
	s_lshl_b32 s22, s96, 3
	s_cmpk_gt_i32 s15, 0x7fff
	s_waitcnt lgkmcnt(0)
	s_barrier
	s_cbranch_scc1 .LBB0_1478
	s_add_u32 s24, s0, 0x12c00000
	s_addc_u32 s25, s1, 0
	s_add_u32 s26, s0, 0x28000000
	s_addc_u32 s27, s1, 0
	s_add_u32 s4, s0, 0x27000000
	s_addc_u32 s5, s1, 0
	s_add_u32 s28, s0, 0x26000000
	s_addc_u32 s29, s1, 0
	s_lshl_b32 s2, s93, 9
	v_and_b32_e32 v159, 64, v6
	s_add_i32 s30, s2, 0
	s_lshl_b32 s2, s93, 8
	v_xor_b32_e32 v0, 16, v6
	v_add_u32_e32 v1, 64, v159
	s_add_i32 s37, s2, 0
	v_cmp_lt_i32_e32 vcc, v0, v1
	s_add_i32 s30, s30, 0x20000
	s_add_i32 s31, s37, 0x21000
	v_cndmask_b32_e32 v0, v6, v0, vcc
	v_lshlrev_b32_e32 v160, 2, v0
	v_xor_b32_e32 v0, 32, v6
	s_add_u32 s33, s0, 0xa000000
	v_cmp_lt_i32_e32 vcc, v0, v1
	s_addc_u32 s34, s1, 0
	s_add_u32 s35, s0, 0x2000000
	v_cndmask_b32_e32 v0, v6, v0, vcc
	s_mov_b32 s7, 0
	v_lshlrev_b32_e32 v161, 2, v0
	s_addc_u32 s36, s1, 0
	s_add_i32 s37, s37, 0x21010
	v_mov_b32_e32 v1, 0
	s_add_i32 s38, 0, 0x24000
	s_mov_b32 s14, 0x3a800000
	s_mov_b32 s39, 0xc3e00000
	s_movk_i32 s40, 0x84
	v_mov_b32_e32 v162, 0x43e00000
	s_lshl_b32 s41, s22, 1
	s_lshl_b32 s42, s22, 5
	s_mov_b32 s43, 0
	v_and_b32_e32 v163, 15, v158
	v_ashrrev_i32_e32 v164, 4, v158
	v_lshl_add_u32 v189, v163, 2, s38
	v_lshlrev_b32_e32 v6, 2, v164
	v_lshlrev_b32_e32 v0, 1, v158
	v_bfe_u32 v5, v158, 2, 2
	v_and_b32_e32 v0, 14, v0
	v_bfe_u32 v4, v158, 3, 1
	v_or_b32_e32 v5, v6, v5
	v_lshlrev_b32_e32 v2, 1, v164
	v_lshlrev_b32_e32 v7, 1, v5
	v_lshlrev_b32_e32 v9, 3, v158
	v_bitop3_b32 v10, v0, v2, v4 bitop3:0x36
	v_or_b32_e32 v11, 1, v2
	v_add_u32_e32 v12, 8, v2
	v_add_u32_e32 v13, 9, v2
	v_add_u32_e32 v14, 16, v2
	v_add_u32_e32 v15, 17, v2
	v_add_u32_e32 v16, 24, v2
	v_add_u32_e32 v2, 25, v2
	v_and_b32_e32 v7, 14, v7
	v_bfe_u32 v8, v164, 1, 1
	v_and_or_b32 v9, v9, 8, s23
	v_bfe_u32 v3, v158, 1, 1
	v_bitop3_b32 v11, v0, v11, v4 bitop3:0x36
	v_bitop3_b32 v12, v0, v12, v4 bitop3:0x36
	v_bitop3_b32 v13, v13, v0, v4 bitop3:0x1e
	v_bitop3_b32 v14, v0, v14, v4 bitop3:0x36
	v_bitop3_b32 v15, v15, v0, v4 bitop3:0x1e
	v_bitop3_b32 v16, v0, v16, v4 bitop3:0x36
	v_bitop3_b32 v0, v2, v0, v4 bitop3:0x1e
	v_lshl_add_u32 v5, v5, 9, v9
	v_lshlrev_b32_e32 v4, 4, v0
	v_bitop3_b32 v0, v7, v3, v8 bitop3:0x36
	v_lshl_add_u32 v177, v0, 4, v5
	v_or_b32_e32 v0, 2, v3
	v_bitop3_b32 v0, v7, v0, v8 bitop3:0x36
	v_lshl_add_u32 v178, v0, 4, v5
	v_or_b32_e32 v0, 4, v3
	v_bitop3_b32 v0, v7, v0, v8 bitop3:0x36
	v_lshl_add_u32 v179, v0, 4, v5
	v_or_b32_e32 v0, 6, v3
	v_bitop3_b32 v0, v7, v0, v8 bitop3:0x36
	v_lshl_add_u32 v180, v0, 4, v5
	v_or_b32_e32 v0, 8, v3
	v_bitop3_b32 v0, v7, v0, v8 bitop3:0x36
	v_lshl_add_u32 v181, v0, 4, v5
	v_or_b32_e32 v0, 10, v3
	v_bitop3_b32 v0, v7, v0, v8 bitop3:0x36
	v_lshl_add_u32 v182, v0, 4, v5
	v_or_b32_e32 v0, 12, v3
	v_bitop3_b32 v0, v7, v0, v8 bitop3:0x36
	v_lshl_add_u32 v183, v0, 4, v5
	v_or_b32_e32 v0, 14, v3
	v_bitop3_b32 v0, v7, v0, v8 bitop3:0x36
	v_lshl_add_u32 v184, v0, 4, v5
	v_or_b32_e32 v0, 16, v3
	v_bitop3_b32 v0, v7, v0, v8 bitop3:0x36
	v_lshl_add_u32 v175, v0, 4, v5
	v_or_b32_e32 v0, 18, v3
	v_bitop3_b32 v0, v7, v0, v8 bitop3:0x36
	v_lshl_add_u32 v176, v0, 4, v5
	v_or_b32_e32 v0, 20, v3
	v_bitop3_b32 v0, v7, v0, v8 bitop3:0x36
	v_lshl_add_u32 v174, v0, 4, v5
	v_or_b32_e32 v0, 22, v3
	v_bitop3_b32 v0, v7, v0, v8 bitop3:0x36
	v_lshl_add_u32 v172, v0, 4, v5
	v_or_b32_e32 v0, 24, v3
	v_bitop3_b32 v0, v7, v0, v8 bitop3:0x36
	v_lshl_add_u32 v173, v0, 4, v5
	v_or_b32_e32 v0, 26, v3
	v_bitop3_b32 v0, v7, v0, v8 bitop3:0x36
	v_lshl_add_u32 v171, v0, 4, v5
	v_or_b32_e32 v0, 28, v3
	v_bitop3_b32 v0, v7, v0, v8 bitop3:0x36
	v_lshl_add_u32 v169, v0, 4, v5
	v_or_b32_e32 v0, 30, v3
	v_bitop3_b32 v0, v7, v0, v8 bitop3:0x36
	v_lshl_add_u32 v9, v163, 9, s23
	v_lshlrev_b32_e32 v10, 4, v10
	v_lshlrev_b32_e32 v11, 4, v11
	v_lshlrev_b32_e32 v12, 4, v12
	v_lshlrev_b32_e32 v13, 4, v13
	v_lshlrev_b32_e32 v14, 4, v14
	v_lshlrev_b32_e32 v15, 4, v15
	v_lshlrev_b32_e32 v16, 4, v16
	v_lshl_add_u32 v170, v0, 4, v5
	v_and_or_b32 v0, v6, 60, v159
	v_lshlrev_b32_e32 v167, 2, v0
	v_add_u32_e32 v193, v9, v10
	v_add_u32_e32 v194, v9, v11
	v_add_u32_e32 v190, v9, v12
	v_add_u32_e32 v191, v9, v13
	v_add_u32_e32 v192, v9, v14
	v_add_u32_e32 v186, v9, v15
	v_add_u32_e32 v187, v9, v16
	v_add_u32_e32 v188, v9, v4
	v_or_b32_e32 v168, 4, v167
	v_or_b32_e32 v165, 8, v167
	v_or_b32_e32 v166, 12, v167
	s_mov_b32 s16, s15
	s_branch .LBB0_1454

.LBB0_1462:
	s_or_b64 exec, exec, s[2:3]
	s_ashr_i32 s19, s18, 31
	s_lshl_b64 s[2:3], s[16:17], 12
	s_add_u32 s44, s24, s2
	s_addc_u32 s45, s25, s3
	v_lshlrev_b32_e32 v0, 8, v163
	v_and_b32_e32 v2, -16, v154
	v_lshl_add_u64 v[8:9], s[44:45], 0, v[0:1]
	v_ashrrev_i32_e32 v3, 31, v2
	v_lshl_add_u64 v[20:21], v[8:9], 0, v[2:3]
	global_load_dwordx4 v[8:11], v[20:21], off nt
	global_load_dwordx4 v[12:15], v[20:21], off offset:64 nt
	global_load_dwordx4 v[16:19], v[20:21], off offset:128 nt
	s_nop 0
	global_load_dwordx4 v[20:23], v[20:21], off offset:192 nt
	s_waitcnt lgkmcnt(0)
	v_or_b32_e32 v0, v6, v4
	v_cmp_ge_i32_e32 vcc, s20, v163
	v_lshl_add_u32 v4, v154, 2, s31
	v_or3_b32 v0, v0, v5, v7
	v_cndmask_b32_e32 v5, 0, v163, vcc
	ds_write_b32 v4, v0
	v_lshl_add_u32 v0, v5, 1, s30
	s_waitcnt lgkmcnt(0)
	ds_read_u16 v0, v0
	s_lshl_b64 s[18:19], s[18:19], 13
	v_lshl_add_u64 v[156:157], s[4:5], 0, v[2:3]
	s_mov_b32 s17, 0
	v_or_b32_e32 v199, 64, v163
	v_mov_b32_e32 v200, 0xff800000
	v_mov_b32_e32 v185, 0
	s_waitcnt vmcnt(3)
	v_cvt_scalef32_pk_bf16_fp8 v66, v8, 1.0
	v_cvt_scalef32_pk_bf16_fp8 v67, v8, 1.0 op_sel:[1,0,0]
	v_cvt_scalef32_pk_bf16_fp8 v68, v9, 1.0
	v_cvt_scalef32_pk_bf16_fp8 v69, v9, 1.0 op_sel:[1,0,0]
	v_or_b32_e32 v4, 16, v163
	v_cmp_ge_i32_e32 vcc, s6, v4
	v_or_b32_e32 v5, 32, v163
	v_cndmask_b32_e32 v4, 0, v4, vcc
	v_cmp_ge_i32_e32 vcc, s6, v5
	v_lshl_add_u32 v4, v4, 1, s30
	v_lshlrev_b32_e32 v6, 2, v164
	v_cndmask_b32_e32 v5, 0, v5, vcc
	v_lshl_add_u32 v5, v5, 1, s30
	v_add_u32_e32 v195, s31, v6
	ds_read_u16 v7, v4
	ds_read_u16 v196, v5
	ds_read_b32 v197, v195
	s_waitcnt lgkmcnt(3)
	v_and_b32_e32 v4, 0xffff, v0
	v_mov_b32_e32 v5, s7
	v_lshl_add_u64 v[4:5], s[18:19], 0, v[4:5]
	v_lshlrev_b64 v[4:5], 8, v[4:5]
	v_lshl_add_u64 v[4:5], s[4:5], 0, v[4:5]
	v_lshl_add_u64 v[4:5], v[4:5], 0, v[2:3]
	global_load_dwordx4 v[110:113], v[4:5], off
	global_load_dwordx4 v[106:109], v[4:5], off offset:64
	global_load_dwordx4 v[102:105], v[4:5], off offset:128
	global_load_dwordx4 v[98:101], v[4:5], off offset:192
	s_waitcnt lgkmcnt(2)
	v_and_b32_e32 v4, 0xffff, v7
	v_mov_b32_e32 v5, s7
	v_lshl_add_u64 v[4:5], s[18:19], 0, v[4:5]
	v_lshlrev_b64 v[4:5], 8, v[4:5]
	v_lshl_add_u64 v[4:5], s[4:5], 0, v[4:5]
	v_lshl_add_u64 v[4:5], v[4:5], 0, v[2:3]
	global_load_dwordx4 v[244:247], v[4:5], off
	global_load_dwordx4 v[240:243], v[4:5], off offset:64
	global_load_dwordx4 v[236:239], v[4:5], off offset:128
	global_load_dwordx4 v[232:235], v[4:5], off offset:192
	v_cvt_scalef32_pk_bf16_fp8 v82, v10, 1.0
	v_cvt_scalef32_pk_bf16_fp8 v83, v10, 1.0 op_sel:[1,0,0]
	v_cvt_scalef32_pk_bf16_fp8 v84, v11, 1.0
	v_cvt_scalef32_pk_bf16_fp8 v85, v11, 1.0 op_sel:[1,0,0]
	s_waitcnt vmcnt(10)
	v_cvt_scalef32_pk_bf16_fp8 v70, v12, 1.0
	v_cvt_scalef32_pk_bf16_fp8 v71, v12, 1.0 op_sel:[1,0,0]
	v_cvt_scalef32_pk_bf16_fp8 v72, v13, 1.0
	v_cvt_scalef32_pk_bf16_fp8 v73, v13, 1.0 op_sel:[1,0,0]
	v_cvt_scalef32_pk_bf16_fp8 v86, v14, 1.0
	v_cvt_scalef32_pk_bf16_fp8 v87, v14, 1.0 op_sel:[1,0,0]
	v_cvt_scalef32_pk_bf16_fp8 v88, v15, 1.0
	v_cvt_scalef32_pk_bf16_fp8 v89, v15, 1.0 op_sel:[1,0,0]
	s_waitcnt vmcnt(9)
	v_cvt_scalef32_pk_bf16_fp8 v74, v16, 1.0
	v_cvt_scalef32_pk_bf16_fp8 v75, v16, 1.0 op_sel:[1,0,0]
	v_cvt_scalef32_pk_bf16_fp8 v76, v17, 1.0
	v_cvt_scalef32_pk_bf16_fp8 v77, v17, 1.0 op_sel:[1,0,0]
	v_cvt_scalef32_pk_bf16_fp8 v90, v18, 1.0
	v_cvt_scalef32_pk_bf16_fp8 v91, v18, 1.0 op_sel:[1,0,0]
	v_cvt_scalef32_pk_bf16_fp8 v92, v19, 1.0
	v_cvt_scalef32_pk_bf16_fp8 v93, v19, 1.0 op_sel:[1,0,0]
	s_waitcnt vmcnt(8)
	v_cvt_scalef32_pk_bf16_fp8 v78, v20, 1.0
	v_cvt_scalef32_pk_bf16_fp8 v79, v20, 1.0 op_sel:[1,0,0]
	v_cvt_scalef32_pk_bf16_fp8 v80, v21, 1.0
	v_cvt_scalef32_pk_bf16_fp8 v81, v21, 1.0 op_sel:[1,0,0]
	v_cvt_scalef32_pk_bf16_fp8 v94, v22, 1.0
	v_cvt_scalef32_pk_bf16_fp8 v95, v22, 1.0 op_sel:[1,0,0]
	v_cvt_scalef32_pk_bf16_fp8 v96, v23, 1.0
	v_cvt_pk_f32_fp8_sdwa v[22:23], v23 src0_sel:WORD_1
	v_mov_b32_e32 v2, v1
	v_mov_b32_e32 v3, v1
	v_cvt_pk_bf16_f32 v97, v22, v23
	v_add_u32_e32 v198, s37, v6
	v_mov_b32_e32 v0, v1
	v_mov_b64_e32 v[64:65], v[2:3]
	v_mov_b64_e32 v[60:61], v[2:3]
	v_mov_b64_e32 v[56:57], v[2:3]
	v_mov_b64_e32 v[52:53], v[2:3]
	v_mov_b64_e32 v[48:49], v[2:3]
	v_mov_b64_e32 v[44:45], v[2:3]
	v_mov_b64_e32 v[40:41], v[2:3]
	v_mov_b64_e32 v[36:37], v[2:3]
	v_mov_b64_e32 v[32:33], v[2:3]
	v_mov_b64_e32 v[28:29], v[2:3]
	v_mov_b64_e32 v[24:25], v[2:3]
	v_mov_b64_e32 v[20:21], v[2:3]
	v_mov_b64_e32 v[16:17], v[2:3]
	v_mov_b64_e32 v[12:13], v[2:3]
	v_mov_b64_e32 v[8:9], v[2:3]
	v_mov_b64_e32 v[62:63], v[0:1]
	v_mov_b64_e32 v[58:59], v[0:1]
	v_mov_b64_e32 v[54:55], v[0:1]
	v_mov_b64_e32 v[50:51], v[0:1]
	v_mov_b64_e32 v[46:47], v[0:1]
	v_mov_b64_e32 v[42:43], v[0:1]
	v_mov_b64_e32 v[38:39], v[0:1]
	v_mov_b64_e32 v[34:35], v[0:1]
	v_mov_b64_e32 v[30:31], v[0:1]
	v_mov_b64_e32 v[26:27], v[0:1]
	v_mov_b64_e32 v[22:23], v[0:1]
	v_mov_b64_e32 v[18:19], v[0:1]
	v_mov_b64_e32 v[14:15], v[0:1]
	v_mov_b64_e32 v[10:11], v[0:1]
	v_mov_b64_e32 v[6:7], v[0:1]
	v_mov_b64_e32 v[4:5], v[2:3]
	v_mov_b64_e32 v[2:3], v[0:1]

.LBB0_1471:
	v_sub_f32_e32 v71, v101, v70
	v_sub_f32_e32 v72, v100, v70
	v_sub_f32_e32 v73, v99, v70
	v_sub_f32_e32 v74, v98, v70
	v_exp_f32_e32 v71, v71
	v_exp_f32_e32 v72, v72
	v_exp_f32_e32 v73, v73
	v_exp_f32_e32 v74, v74
	v_sub_f32_e32 v69, v69, v70
	v_sub_f32_e32 v68, v68, v70
	v_sub_f32_e32 v67, v67, v70
	v_sub_f32_e32 v66, v66, v70
	v_exp_f32_e32 v69, v69
	v_exp_f32_e32 v68, v68
	v_exp_f32_e32 v77, v67
	v_exp_f32_e32 v70, v66
	v_add_f32_e32 v75, v71, v72
	v_add_f32_e32 v76, v73, v74
	v_add_f32_e32 v66, v75, v76
	v_fmac_f32_e32 v66, v185, v0
	v_add_f32_e32 v0, v69, v68
	v_add_f32_e32 v67, v77, v70
	v_add_f32_e32 v0, v0, v67
	v_add_f32_e32 v0, v0, v66
	v_cvt_pk_bf16_f32 v66, v71, v72
	v_cvt_pk_bf16_f32 v68, v69, v68
	v_cvt_pk_bf16_f32 v69, v77, v70
	ds_read_b64_tr_b16 v[70:71],v177
	v_cvt_pk_bf16_f32 v67, v73, v74
	ds_read_b64_tr_b16 v[72:73],v177 offset:8192
	ds_read_b64_tr_b16 v[74:75],v178
	ds_read_b64_tr_b16 v[76:77],v178 offset:8192
	ds_read_b64_tr_b16 v[78:79],v179
	ds_read_b64_tr_b16 v[80:81],v179 offset:8192
	ds_read_b64_tr_b16 v[82:83],v180
	ds_read_b64_tr_b16 v[84:85],v180 offset:8192
	ds_read_b64_tr_b16 v[86:87],v181
	ds_read_b64_tr_b16 v[88:89],v181 offset:8192
	ds_read_b64_tr_b16 v[90:91],v182
	ds_read_b64_tr_b16 v[92:93],v182 offset:8192
	ds_read_b64_tr_b16 v[94:95],v183
	ds_read_b64_tr_b16 v[96:97],v183 offset:8192
	ds_read_b64_tr_b16 v[98:99],v184
	ds_read_b64_tr_b16 v[100:101],v184 offset:8192
	s_waitcnt lgkmcnt(0)
	s_nop 1
	v_mfma_f32_16x16x32_bf16 v[62:65], v[66:69], v[70:73], v[62:65]
	ds_read_b64_tr_b16 v[70:71],v175
	ds_read_b64_tr_b16 v[72:73],v175 offset:8192
	v_mfma_f32_16x16x32_bf16 v[58:61], v[66:69], v[74:77], v[58:61]
	ds_read_b64_tr_b16 v[74:75],v176
	ds_read_b64_tr_b16 v[76:77],v176 offset:8192
	v_mfma_f32_16x16x32_bf16 v[54:57], v[66:69], v[78:81], v[54:57]
	ds_read_b64_tr_b16 v[78:79],v174
	ds_read_b64_tr_b16 v[80:81],v174 offset:8192
	v_mfma_f32_16x16x32_bf16 v[50:53], v[66:69], v[82:85], v[50:53]
	ds_read_b64_tr_b16 v[82:83],v172
	ds_read_b64_tr_b16 v[84:85],v172 offset:8192
	v_mfma_f32_16x16x32_bf16 v[46:49], v[66:69], v[86:89], v[46:49]
	ds_read_b64_tr_b16 v[86:87],v173
	ds_read_b64_tr_b16 v[88:89],v173 offset:8192
	v_mfma_f32_16x16x32_bf16 v[42:45], v[66:69], v[90:93], v[42:45]
	ds_read_b64_tr_b16 v[90:91],v171
	ds_read_b64_tr_b16 v[92:93],v171 offset:8192
	ds_read_b64_tr_b16 v[102:103],v169
	ds_read_b64_tr_b16 v[104:105],v169 offset:8192
	v_mfma_f32_16x16x32_bf16 v[38:41], v[66:69], v[94:97], v[38:41]
	ds_read_b64_tr_b16 v[94:95],v170
	ds_read_b64_tr_b16 v[96:97],v170 offset:8192
	s_waitcnt lgkmcnt(0)
	v_mfma_f32_16x16x32_bf16 v[34:37], v[66:69], v[98:101], v[34:37]
	v_mfma_f32_16x16x32_bf16 v[30:33], v[66:69], v[70:73], v[30:33]
	ds_bpermute_b32 v70, v160, v0
	s_waitcnt lgkmcnt(0)
	s_add_u32 s2, s26, s2
	v_mfma_f32_16x16x32_bf16 v[26:29], v[66:69], v[74:77], v[26:29]
	s_addc_u32 s3, s27, s3
	s_waitcnt lgkmcnt(0)
	v_add_f32_e32 v0, v0, v70
	ds_bpermute_b32 v70, v161, v0
	v_mfma_f32_16x16x32_bf16 v[22:25], v[66:69], v[78:81], v[22:25]
	s_lshl_b32 s17, s15, 1
	s_lshl_b32 s44, s15, 5
	s_mov_b32 s45, -1
	s_waitcnt lgkmcnt(0)
	v_add_f32_e32 v0, v0, v70
	v_div_scale_f32 v70, s[18:19], v0, v0, 1.0
	v_rcp_f32_e32 v71, v70
	v_div_scale_f32 v72, vcc, 1.0, v0, 1.0
	v_mfma_f32_16x16x32_bf16 v[18:21], v[66:69], v[82:85], v[18:21]
	v_fma_f32 v73, -v70, v71, 1.0
	v_fmac_f32_e32 v71, v73, v71
	v_mul_f32_e32 v73, v72, v71
	v_fma_f32 v74, -v70, v73, v72
	v_fmac_f32_e32 v73, v74, v71
	v_fma_f32 v70, -v70, v73, v72
	v_div_fmas_f32 v70, v70, v71, v73
	v_div_fixup_f32 v0, v70, v0, 1.0
	ds_bpermute_b32 v71, v168, v0
	ds_bpermute_b32 v72, v165, v0
	ds_bpermute_b32 v70, v167, v0
	ds_bpermute_b32 v0, v166, v0
	v_mfma_f32_16x16x32_bf16 v[14:17], v[66:69], v[86:89], v[14:17]
	s_waitcnt lgkmcnt(3)
	v_mul_f32_e32 v63, v63, v71
	v_med3_f32 v63, v63, s39, v162
	s_waitcnt lgkmcnt(1)
	v_mul_f32_e32 v58, v58, v70
	v_mfma_f32_16x16x32_bf16 v[10:13], v[66:69], v[90:93], v[10:13]
	v_med3_f32 v58, v58, s39, v162
	v_mul_f32_e32 v54, v54, v70
	v_med3_f32 v54, v54, s39, v162
	v_mfma_f32_16x16x32_bf16 v[6:9], v[66:69], v[102:105], v[6:9]
	v_mul_f32_e32 v50, v50, v70
	v_med3_f32 v50, v50, s39, v162
	v_mul_f32_e32 v46, v46, v70
	v_mfma_f32_16x16x32_bf16 v[2:5], v[66:69], v[94:97], v[2:5]
	v_cvt_pk_fp8_f32 v67, v63, 0
	v_mul_f32_e32 v63, v64, v72
	v_med3_f32 v63, v63, s39, v162
	v_cvt_pk_fp8_f32 v64, v63, 0
	s_waitcnt lgkmcnt(0)
	v_mul_f32_e32 v63, v65, v0
	v_med3_f32 v63, v63, s39, v162
	v_cvt_pk_fp8_f32 v65, v63, 0
	v_cvt_pk_fp8_f32 v63, v58, 0
	v_mul_f32_e32 v58, v59, v71
	v_med3_f32 v58, v58, s39, v162
	v_cvt_pk_fp8_f32 v59, v58, 0
	v_mul_f32_e32 v58, v60, v72
	v_med3_f32 v58, v58, s39, v162
	v_cvt_pk_fp8_f32 v60, v58, 0
	v_mul_f32_e32 v58, v61, v0
	v_med3_f32 v58, v58, s39, v162
	v_cvt_pk_fp8_f32 v61, v58, 0
	v_cvt_pk_fp8_f32 v58, v54, 0
	v_mul_f32_e32 v54, v55, v71
	v_med3_f32 v54, v54, s39, v162
	v_cvt_pk_fp8_f32 v55, v54, 0
	v_mul_f32_e32 v54, v56, v72
	v_med3_f32 v54, v54, s39, v162
	v_cvt_pk_fp8_f32 v56, v54, 0
	v_mul_f32_e32 v54, v57, v0
	v_med3_f32 v54, v54, s39, v162
	v_cvt_pk_fp8_f32 v57, v54, 0
	v_cvt_pk_fp8_f32 v54, v50, 0
	v_mul_f32_e32 v50, v51, v71
	v_med3_f32 v50, v50, s39, v162
	v_cvt_pk_fp8_f32 v51, v50, 0
	v_mul_f32_e32 v50, v52, v72
	v_med3_f32 v50, v50, s39, v162
	v_cvt_pk_fp8_f32 v52, v50, 0
	v_mul_f32_e32 v50, v53, v0
	v_med3_f32 v50, v50, s39, v162
	v_cvt_pk_fp8_f32 v53, v50, 0
	v_med3_f32 v46, v46, s39, v162
	v_cvt_pk_fp8_f32 v50, v46, 0
	v_mul_f32_e32 v46, v47, v71
	v_med3_f32 v46, v46, s39, v162
	v_cvt_pk_fp8_f32 v47, v46, 0
	v_mul_f32_e32 v46, v48, v72
	v_med3_f32 v46, v46, s39, v162
	v_cvt_pk_fp8_f32 v48, v46, 0
	v_mul_f32_e32 v46, v49, v0
	v_med3_f32 v46, v46, s39, v162
	v_mul_f32_e32 v42, v42, v70
	v_cvt_pk_fp8_f32 v49, v46, 0
	v_med3_f32 v42, v42, s39, v162
	v_mov_b32_e32 v46, v1
	v_cvt_pk_fp8_f32 v46, v42, 0
	v_mul_f32_e32 v42, v43, v71
	v_med3_f32 v42, v42, s39, v162
	v_mov_b32_e32 v43, v1
	v_cvt_pk_fp8_f32 v43, v42, 0
	v_mul_f32_e32 v42, v44, v72
	v_med3_f32 v42, v42, s39, v162
	v_mov_b32_e32 v44, v1
	v_cvt_pk_fp8_f32 v44, v42, 0
	v_mul_f32_e32 v42, v45, v0
	v_med3_f32 v42, v42, s39, v162
	v_mov_b32_e32 v45, v1
	v_mul_f32_e32 v38, v38, v70
	v_cvt_pk_fp8_f32 v45, v42, 0
	v_med3_f32 v38, v38, s39, v162
	v_mov_b32_e32 v42, v1
	v_cvt_pk_fp8_f32 v42, v38, 0
	v_mul_f32_e32 v38, v39, v71
	v_med3_f32 v38, v38, s39, v162
	v_mov_b32_e32 v39, v1
	v_cvt_pk_fp8_f32 v39, v38, 0
	v_mul_f32_e32 v38, v40, v72
	v_med3_f32 v38, v38, s39, v162
	v_mov_b32_e32 v40, v1
	v_cvt_pk_fp8_f32 v40, v38, 0
	v_mul_f32_e32 v38, v41, v0
	v_med3_f32 v38, v38, s39, v162
	v_mov_b32_e32 v41, v1
	v_mul_f32_e32 v34, v34, v70
	v_cvt_pk_fp8_f32 v41, v38, 0
	v_med3_f32 v34, v34, s39, v162
	v_mov_b32_e32 v38, v1
	v_cvt_pk_fp8_f32 v38, v34, 0
	v_mul_f32_e32 v34, v35, v71
	v_med3_f32 v34, v34, s39, v162
	v_mov_b32_e32 v35, v1
	v_cvt_pk_fp8_f32 v35, v34, 0
	v_mul_f32_e32 v34, v36, v72
	v_med3_f32 v34, v34, s39, v162
	v_mov_b32_e32 v36, v1
	v_cvt_pk_fp8_f32 v36, v34, 0
	v_mul_f32_e32 v34, v37, v0
	v_med3_f32 v34, v34, s39, v162
	v_mov_b32_e32 v37, v1
	v_mul_f32_e32 v30, v30, v70
	v_cvt_pk_fp8_f32 v37, v34, 0
	v_med3_f32 v30, v30, s39, v162
	v_mov_b32_e32 v34, v1
	v_cvt_pk_fp8_f32 v34, v30, 0
	v_mul_f32_e32 v30, v31, v71
	v_med3_f32 v30, v30, s39, v162
	v_cvt_pk_fp8_f32 v31, v30, 0
	v_mul_f32_e32 v30, v32, v72
	v_med3_f32 v30, v30, s39, v162
	v_mov_b32_e32 v32, v1
	v_cvt_pk_fp8_f32 v32, v30, 0
	v_mul_f32_e32 v30, v33, v0
	v_med3_f32 v30, v30, s39, v162
	v_mov_b32_e32 v33, v1
	v_mul_f32_e32 v26, v26, v70
	v_cvt_pk_fp8_f32 v33, v30, 0
	v_med3_f32 v26, v26, s39, v162
	v_cvt_pk_fp8_f32 v30, v26, 0
	v_mul_f32_e32 v26, v27, v71
	v_med3_f32 v26, v26, s39, v162
	v_cvt_pk_fp8_f32 v27, v26, 0
	v_mul_f32_e32 v26, v28, v72
	v_med3_f32 v26, v26, s39, v162
	v_cvt_pk_fp8_f32 v28, v26, 0
	v_mul_f32_e32 v26, v29, v0
	v_med3_f32 v26, v26, s39, v162
	v_mul_f32_e32 v22, v22, v70
	v_cvt_pk_fp8_f32 v29, v26, 0
	v_med3_f32 v22, v22, s39, v162
	v_cvt_pk_fp8_f32 v26, v22, 0
	v_mul_f32_e32 v22, v23, v71
	v_med3_f32 v22, v22, s39, v162
	v_cvt_pk_fp8_f32 v23, v22, 0
	v_mul_f32_e32 v22, v24, v72
	v_med3_f32 v22, v22, s39, v162
	v_cvt_pk_fp8_f32 v24, v22, 0
	v_mul_f32_e32 v22, v25, v0
	v_med3_f32 v22, v22, s39, v162
	v_mul_f32_e32 v18, v18, v70
	v_cvt_pk_fp8_f32 v25, v22, 0
	v_med3_f32 v18, v18, s39, v162
	v_cvt_pk_fp8_f32 v22, v18, 0
	v_mul_f32_e32 v18, v19, v71
	v_med3_f32 v18, v18, s39, v162
	v_cvt_pk_fp8_f32 v19, v18, 0
	v_mul_f32_e32 v18, v20, v72
	v_med3_f32 v18, v18, s39, v162
	v_cvt_pk_fp8_f32 v20, v18, 0
	v_mul_f32_e32 v18, v21, v0
	v_med3_f32 v18, v18, s39, v162
	v_mul_f32_e32 v14, v14, v70
	v_cvt_pk_fp8_f32 v21, v18, 0
	v_med3_f32 v14, v14, s39, v162
	v_cvt_pk_fp8_f32 v18, v14, 0
	v_mul_f32_e32 v14, v15, v71
	v_med3_f32 v14, v14, s39, v162
	v_cvt_pk_fp8_f32 v15, v14, 0
	v_mul_f32_e32 v14, v16, v72
	v_med3_f32 v14, v14, s39, v162
	v_cvt_pk_fp8_f32 v16, v14, 0
	v_mul_f32_e32 v14, v17, v0
	v_med3_f32 v14, v14, s39, v162
	v_mul_f32_e32 v10, v10, v70
	v_cvt_pk_fp8_f32 v17, v14, 0
	v_med3_f32 v10, v10, s39, v162
	v_cvt_pk_fp8_f32 v14, v10, 0
	v_mul_f32_e32 v10, v11, v71
	v_med3_f32 v10, v10, s39, v162
	v_cvt_pk_fp8_f32 v11, v10, 0
	v_mul_f32_e32 v10, v12, v72
	v_med3_f32 v10, v10, s39, v162
	v_cvt_pk_fp8_f32 v12, v10, 0
	v_mul_f32_e32 v10, v13, v0
	v_med3_f32 v10, v10, s39, v162
	v_mul_f32_e32 v6, v6, v70
	v_cvt_pk_fp8_f32 v13, v10, 0
	v_med3_f32 v6, v6, s39, v162
	v_cvt_pk_fp8_f32 v10, v6, 0
	v_mul_f32_e32 v6, v7, v71
	v_med3_f32 v6, v6, s39, v162
	v_cvt_pk_fp8_f32 v7, v6, 0
	v_mul_f32_e32 v6, v8, v72
	v_med3_f32 v6, v6, s39, v162
	v_cvt_pk_fp8_f32 v8, v6, 0
	v_mul_f32_e32 v6, v9, v0
	v_med3_f32 v6, v6, s39, v162
	v_mul_f32_e32 v2, v2, v70
	v_cvt_pk_fp8_f32 v9, v6, 0
	v_med3_f32 v2, v2, s39, v162
	v_mul_f32_e32 v62, v62, v70
	v_cvt_pk_fp8_f32 v6, v2, 0
	v_mul_f32_e32 v2, v3, v71
	v_med3_f32 v62, v62, s39, v162
	v_med3_f32 v2, v2, s39, v162
	v_cvt_pk_fp8_f32 v66, v62, 0
	v_cvt_pk_fp8_f32 v3, v2, 0
	v_mul_f32_e32 v2, v4, v72
	v_med3_f32 v2, v2, s39, v162
	v_mul_f32_e32 v0, v5, v0
	v_lshlrev_b32_e32 v62, 10, v164
	v_cvt_pk_fp8_f32 v4, v2, 0
	v_med3_f32 v0, v0, s39, v162
	v_add3_u32 v62, s23, v163, v62
	v_cvt_pk_fp8_f32 v2, v0, 0
	ds_write_b8 v62, v66
	ds_write_b8 v62, v67 offset:256
	ds_write_b8 v62, v64 offset:512
	ds_write_b8 v62, v65 offset:768
	ds_write_b8 v62, v63 offset:16
	ds_write_b8 v62, v59 offset:272
	ds_write_b8 v62, v60 offset:528
	ds_write_b8 v62, v61 offset:784
	ds_write_b8 v62, v58 offset:32
	ds_write_b8 v62, v55 offset:288
	ds_write_b8 v62, v56 offset:544
	ds_write_b8 v62, v57 offset:800
	ds_write_b8 v62, v54 offset:48
	ds_write_b8 v62, v51 offset:304
	ds_write_b8 v62, v52 offset:560
	ds_write_b8 v62, v53 offset:816
	ds_write_b8 v62, v50 offset:64
	ds_write_b8 v62, v47 offset:320
	ds_write_b8 v62, v48 offset:576
	ds_write_b8 v62, v49 offset:832
	ds_write_b8 v62, v46 offset:80
	ds_write_b8 v62, v43 offset:336
	ds_write_b8 v62, v44 offset:592
	ds_write_b8 v62, v45 offset:848
	ds_write_b8 v62, v42 offset:96
	ds_write_b8 v62, v39 offset:352
	ds_write_b8 v62, v40 offset:608
	ds_write_b8 v62, v41 offset:864
	ds_write_b8 v62, v38 offset:112
	ds_write_b8 v62, v35 offset:368
	ds_write_b8 v62, v36 offset:624
	ds_write_b8 v62, v37 offset:880
	ds_write_b8 v62, v34 offset:128
	ds_write_b8 v62, v31 offset:384
	ds_write_b8 v62, v32 offset:640
	ds_write_b8 v62, v33 offset:896
	ds_write_b8 v62, v30 offset:144
	ds_write_b8 v62, v27 offset:400
	ds_write_b8 v62, v28 offset:656
	ds_write_b8 v62, v29 offset:912
	ds_write_b8 v62, v26 offset:160
	ds_write_b8 v62, v23 offset:416
	ds_write_b8 v62, v24 offset:672
	ds_write_b8 v62, v25 offset:928
	ds_write_b8 v62, v22 offset:176
	ds_write_b8 v62, v19 offset:432
	ds_write_b8 v62, v20 offset:688
	ds_write_b8 v62, v21 offset:944
	ds_write_b8 v62, v18 offset:192
	ds_write_b8 v62, v15 offset:448
	ds_write_b8 v62, v16 offset:704
	ds_write_b8 v62, v17 offset:960
	ds_write_b8 v62, v14 offset:208
	ds_write_b8 v62, v11 offset:464
	ds_write_b8 v62, v12 offset:720
	ds_write_b8 v62, v13 offset:976
	ds_write_b8 v62, v10 offset:224
	ds_write_b8 v62, v7 offset:480
	ds_write_b8 v62, v8 offset:736
	ds_write_b8 v62, v9 offset:992
	ds_write_b8 v62, v6 offset:240
	ds_write_b8 v62, v3 offset:496
	ds_write_b8 v62, v4 offset:752
	ds_write_b8 v62, v2 offset:1008
	s_waitcnt lgkmcnt(0)
	v_lshl_add_u32 v0, v154, 4, s23
	ds_read_b128 v[2:5], v0
	ds_read_b128 v[6:9], v0 offset:1024
	ds_read_b128 v[10:13], v0 offset:2048
	ds_read_b128 v[14:17], v0 offset:3072
	v_lshl_add_u64 v[18:19], v[154:155], 4, s[2:3]
	s_waitcnt lgkmcnt(3)
	global_store_dwordx4 v[18:19], v[2:5], off nt
	s_waitcnt lgkmcnt(2)
	global_store_dwordx4 v[18:19], v[6:9], off offset:1024 nt
	s_waitcnt lgkmcnt(1)
	global_store_dwordx4 v[18:19], v[10:13], off offset:2048 nt
	s_waitcnt lgkmcnt(0)
	global_store_dwordx4 v[18:19], v[14:17], off offset:3072 nt
	s_waitcnt lgkmcnt(0)
	s_branch .LBB0_1473
